# in-proj GEMM on 188 workgroups (was 180), gate/up conversion on 68
# baseline (speedup 1.0000x reference)
; #define LAS __attribute__((address_space(3)))
; __device__ __forceinline__ void wout_transpose(const Params& p, Frame& F, int gw, int NGW) {
;     LAS unsigned char* tile = F.lds + 16384 + F.wave * 16384;
;     __syncthreads();
;     for (int it = gw; it < (DM / 128) * (DM / 64); it += NGW) {
;         const int nb = it % (DM / 64), kb = it / (DM / 64); p0_transpose_item_bf16(p.in[10], DM, kb * 128, nb * 64, (bf16_t*)(p.ws + WS_WOUT), DM, nb * 64, nullptr, tile, F.lane);
; __global__ void __launch_bounds__(512, 2) hymba_fwd(Params p) {
;     ...
;         const int ng = (F.G == 256) ? NG_GEMM : F.G;
;         if ((int)blockIdx.x < ng) {
;             pg8::Gemm g{(const bf16_t*)(ws + WS_XB), (const bf16_t*)(ws + WS_WIN), DM}; pg8::StaticOrder S; S.init(T_TOK, NPROJ, ng, (int)blockIdx.x);
;             EpiProj E{(bf16_t*)(ws + WS_PROJ), (const float*)(ws + WS_RSTD1)};
;             pg8::gemm_phase<EpiProj, pg8::StaticOrder, false, false, true, false>(ring, g, S, E);
;             if (ng == F.G) { wout_transpose(p, F, (int)blockIdx.x * 8 + F.wave, F.G * 8); moe_weight_convert(p, F, (int)blockIdx.x * 8 + F.wave, F.G * 8, 0, CONV_N_GU); }
;         } else { wout_transpose(p, F, ((int)blockIdx.x - ng) * 8 + F.wave, (F.G - ng) * 8); moe_weight_convert(p, F, ((int)blockIdx.x - ng) * 8 + F.wave, (F.G - ng) * 8, 0, CONV_N_GU); }
.LBB0_145:
	v_readlane_b32 s4, v245, 4
	s_cmp_lt_i32 s4, 2
	s_cselect_b64 s[0:1], -1, 0
	s_and_b64 s[2:3], s[0:1], s[2:3]
	s_andn2_b64 vcc, exec, s[2:3]
	v_readlane_b32 s5, v245, 5
	v_readlane_b32 s6, v245, 6
	v_readlane_b32 s7, v245, 7
	s_cbranch_vccnz .LBB0_233
	s_cmpk_lg_i32 s94, 0x100
	s_cselect_b64 s[12:13], -1, 0
	s_and_b64 s[2:3], s[12:13], exec
	s_cselect_b32 s20, s94, 0xbc
	v_readlane_b32 s2, v245, 18
	s_cmp_ge_i32 s2, s20
	s_mov_b64 s[2:3], -1
	s_cbranch_scc0 .LBB0_182
	v_readlane_b32 s2, v245, 18
	s_sub_i32 s2, s2, s20
	s_lshl_b32 s6, s2, 3
	s_sub_i32 s2, s94, s20
	s_add_i32 s6, s6, s54
	s_lshl_b32 s21, s2, 3
	v_readlane_b32 s56, v245, 39
	s_cmpk_gt_u32 s6, 0x1ff
	v_readlane_b32 s60, v245, 43
	v_readlane_b32 s61, v245, 44
	v_readlane_b32 s62, v245, 45
	v_readlane_b32 s63, v245, 46
	s_barrier
	v_readlane_b32 s57, v245, 40
	v_readlane_b32 s58, v245, 41
	v_readlane_b32 s59, v245, 42
	v_readlane_b32 s64, v245, 47
	v_readlane_b32 s65, v245, 48
	v_readlane_b32 s66, v245, 49
	v_readlane_b32 s67, v245, 50
	v_readlane_b32 s68, v245, 51
	v_readlane_b32 s69, v245, 52
	v_readlane_b32 s70, v245, 53
	v_readlane_b32 s71, v245, 54
	s_cbranch_scc1 .LBB0_150
	s_lshl_b32 s2, s54, 14
	v_lshrrev_b32_e32 v5, 1, v162
	s_add_i32 s4, s2, 0
	v_and_b32_e32 v2, 15, v0
	v_lshrrev_b32_e32 v4, 5, v162
	v_and_b32_e32 v5, 8, v5
	v_lshrrev_b32_e32 v1, 4, v162
	v_lshlrev_b32_e32 v8, 2, v2
	v_mov_b32_e32 v3, 0
	v_add_u32_e32 v5, s4, v5
	v_bitop3_b32 v7, v4, v0, 15 bitop3:0x78
	v_lshlrev_b32_e32 v9, 10, v2
	v_bitop3_b32 v10, v4, v2, 2 bitop3:0x36
	v_bitop3_b32 v11, v4, v2, 4 bitop3:0x36
	v_bitop3_b32 v12, v4, v2, 6 bitop3:0x36
	v_bitop3_b32 v13, v4, v2, 8 bitop3:0x36
	v_bitop3_b32 v14, v4, v2, 10 bitop3:0x36
	v_bitop3_b32 v15, v4, v2, 12 bitop3:0x36
	v_bitop3_b32 v4, v4, v2, 14 bitop3:0x36
	v_lshlrev_b32_e32 v2, 4, v2
	v_lshl_add_u32 v7, v7, 4, v5
	v_lshl_add_u32 v10, v10, 4, v5
	v_lshl_add_u32 v11, v11, 4, v5
	v_lshl_add_u32 v12, v12, 4, v5
	v_lshl_add_u32 v13, v13, 4, v5
	v_lshl_add_u32 v14, v14, 4, v5
	v_lshl_add_u32 v15, v15, 4, v5
	v_lshl_add_u32 v16, v4, 4, v5
	v_lshl_add_u64 v[4:5], s[96:97], 0, v[2:3]
	v_lshl_add_u32 v17, v1, 8, s4
	v_lshlrev_b32_e32 v2, 4, v0
	v_mov_b32_e32 v20, 0xf0
	s_movk_i32 s4, 0x80
	v_bitop3_b32 v35, v2, s4, v20 bitop3:0x6c
	s_movk_i32 s4, 0x90
	v_bitop3_b32 v37, v2, s4, v20 bitop3:0x6c
	s_movk_i32 s4, 0xa0
	s_mov_b64 s[2:3], 0x31000000
	v_bitop3_b32 v39, v2, s4, v20 bitop3:0x6c
	s_movk_i32 s4, 0xb0
	v_lshl_add_u64 v[4:5], v[4:5], 0, s[2:3]
	s_movk_i32 s2, 0x50
	v_bitop3_b32 v41, v2, s4, v20 bitop3:0x6c
	s_movk_i32 s4, 0xc0
	v_bitop3_b32 v29, v2, s2, v20 bitop3:0x6c
	s_movk_i32 s2, 0x60
	v_bitop3_b32 v43, v2, s4, v20 bitop3:0x6c
	s_movk_i32 s4, 0xd0
	s_movk_i32 s3, 0xf0
	v_bitop3_b32 v31, v2, s2, v20 bitop3:0x6c
	s_movk_i32 s2, 0x70
	v_bitop3_b32 v45, v2, s4, v20 bitop3:0x6c
	s_movk_i32 s4, 0xe0
	v_and_b32_e32 v18, 0xf0, v2
	v_add_u32_e32 v19, 0x400, v17
	v_bitop3_b32 v21, v2, 16, v20 bitop3:0x6c
	v_add_u32_e32 v22, 0x800, v17
	v_bitop3_b32 v23, v2, 32, v20 bitop3:0x6c
	v_add_u32_e32 v24, 0xc00, v17
	v_bitop3_b32 v25, v2, 48, v20 bitop3:0x6c
	v_add_u32_e32 v26, 0x1000, v17
	v_bitop3_b32 v27, v2, 64, v20 bitop3:0x6c
	v_add_u32_e32 v28, 0x1400, v17
	v_add_u32_e32 v30, 0x1800, v17
	v_add_u32_e32 v32, 0x1c00, v17
	v_bitop3_b32 v33, v2, s2, v20 bitop3:0x6c
	v_add_u32_e32 v34, 0x2000, v17
	v_add_u32_e32 v36, 0x2400, v17
	v_add_u32_e32 v38, 0x2800, v17
	v_add_u32_e32 v40, 0x2c00, v17
	v_add_u32_e32 v42, 0x3000, v17
	v_add_u32_e32 v44, 0x3400, v17
	v_add_u32_e32 v46, 0x3800, v17
	v_bitop3_b32 v47, v2, s4, v20 bitop3:0x6c
	v_add_u32_e32 v48, 0x3c00, v17
	v_bitop3_b32 v49, v2, s3, v2 bitop3:0xc
	v_add_u32_e32 v50, v7, v9
	v_add_u32_e32 v51, v10, v9
	v_add_u32_e32 v52, v11, v9
	v_add_u32_e32 v53, v12, v9
	v_add_u32_e32 v54, v13, v9
	v_add_u32_e32 v55, v14, v9
	v_add_u32_e32 v56, v15, v9
	v_add_u32_e32 v57, v16, v9
	v_lshlrev_b32_e32 v6, 2, v1
	s_movk_i32 s2, 0x2000
	s_lshl_b32 s3, s6, 6
	s_lshl_b32 s4, s21, 6
	v_lshlrev_b32_e32 v2, 2, v8
	s_movk_i32 s5, 0x4000
	s_movk_i32 s7, 0x6000
	s_mov_b32 s8, 0x20000
	s_mov_b32 s9, 0x22000
	s_mov_b32 s10, 0x24000
	s_mov_b32 s11, 0x26000
	s_mov_b32 s14, 0x40000
	s_mov_b32 s15, 0x42000
	s_mov_b32 s16, 0x44000
	s_mov_b32 s17, 0x46000
	s_mov_b32 s18, 0x60000
	s_mov_b32 s19, 0x62000
	s_mov_b32 s22, 0x64000
	s_mov_b32 s23, 0x66000
	s_mov_b32 s24, 0x80000
	s_mov_b32 s25, 0x82000
	s_mov_b32 s26, 0x84000
	s_mov_b32 s27, 0x86000
	s_mov_b32 s28, 0xa0000
	s_mov_b32 s29, 0xa2000
	s_mov_b32 s30, 0xa4000
	s_mov_b32 s31, 0xa6000
	s_mov_b32 s33, 0xc0000
	s_mov_b32 s34, 0xc2000
	s_mov_b32 s35, 0xc4000
	s_mov_b32 s36, 0xc6000
	s_mov_b32 s37, 0xe0000
	s_mov_b32 s38, 0xe2000
	s_mov_b32 s39, 0xe4000
	s_mov_b32 s40, 0xe6000
	v_add_u32_e32 v7, v17, v18
	v_add_u32_e32 v8, v19, v21
	v_add_u32_e32 v9, v22, v23
	v_add_u32_e32 v10, v24, v25
	v_add_u32_e32 v11, v26, v27
	v_add_u32_e32 v12, v28, v29
	v_add_u32_e32 v13, v30, v31
	v_add_u32_e32 v14, v32, v33
	v_add_u32_e32 v15, v34, v35
	v_add_u32_e32 v16, v36, v37
	v_add_u32_e32 v17, v38, v39
	v_add_u32_e32 v18, v40, v41
	v_add_u32_e32 v19, v42, v43
	v_add_u32_e32 v20, v44, v45
	v_add_u32_e32 v21, v46, v47
	v_add_u32_e32 v22, v48, v49
	v_add_u32_e32 v23, 0x4000, v50
	v_add_u32_e32 v24, 0x4000, v51
	v_add_u32_e32 v25, 0x4000, v52
	v_add_u32_e32 v26, 0x4000, v53
	v_add_u32_e32 v27, 0x4000, v54
	v_add_u32_e32 v28, 0x4000, v55
	v_add_u32_e32 v29, 0x4000, v56
	v_add_u32_e32 v30, 0x4000, v57
	s_mov_b32 s41, s6
